# v11
# speedup vs baseline: 1.0289x; 1.0060x over previous
.LBB2_35:
	s_lshl_b32 s28, s27, 2
	v_add_u32_e32 v79, s28, v3
	v_lshl_add_u32 v79, v79, 2, v2
	ds_read_b32 v80, v79 offset:15360
	ds_read_b32 v81, v79 offset:15364
	ds_read_b32 v82, v79 offset:15368
	ds_read_b32 v79, v79 offset:15372
	s_waitcnt vmcnt(10)
	v_cvt_pk_f16_f32 v10, v61, v62
	v_perm_b32 v11, v40, v38, s23
	v_dot2c_f32_f16_e32 v60, v11, v10
	v_perm_b32 v11, v40, v38, s24
	v_dot2c_f32_f16_e32 v42, v11, v10
	v_perm_b32 v11, v40, v38, s25
	v_dot2c_f32_f16_e32 v43, v11, v10
	v_perm_b32 v11, v40, v38, s26
	v_dot2c_f32_f16_e32 v36, v11, v10
	v_perm_b32 v11, v41, v39, s23
	v_dot2c_f32_f16_e32 v37, v11, v10
	v_perm_b32 v11, v41, v39, s24
	v_dot2c_f32_f16_e32 v30, v11, v10
	v_perm_b32 v11, v41, v39, s25
	v_dot2c_f32_f16_e32 v31, v11, v10
	v_perm_b32 v11, v41, v39, s26
	v_dot2c_f32_f16_e32 v53, v11, v10
	v_dot2c_f32_f16_e32 v45, 0x3c003c00, v10
	s_waitcnt vmcnt(8)
	v_cvt_pk_f16_f32 v10, v58, v59
	v_perm_b32 v11, v34, v32, s23
	v_dot2c_f32_f16_e32 v60, v11, v10
	v_perm_b32 v11, v34, v32, s24
	v_dot2c_f32_f16_e32 v42, v11, v10
	v_perm_b32 v11, v34, v32, s25
	v_dot2c_f32_f16_e32 v43, v11, v10
	v_perm_b32 v11, v34, v32, s26
	v_dot2c_f32_f16_e32 v36, v11, v10
	v_perm_b32 v11, v35, v33, s23
	v_dot2c_f32_f16_e32 v37, v11, v10
	v_perm_b32 v11, v35, v33, s24
	v_dot2c_f32_f16_e32 v30, v11, v10
	v_perm_b32 v11, v35, v33, s25
	v_dot2c_f32_f16_e32 v31, v11, v10
	v_perm_b32 v11, v35, v33, s26
	s_add_i32 s5, s5, 1
	v_dot2c_f32_f16_e32 v53, v11, v10
	s_cmp_lg_u32 s5, s4
	v_dot2c_f32_f16_e32 v45, 0x3c003c00, v10
	s_cbranch_scc1 .LBB2_43
	v_cmp_gt_i32_e32 vcc, 15, v18
	s_and_saveexec_b64 s[4:5], vcc
	s_cbranch_execz .LBB2_38
	v_max_i32_e32 v10, 1, v44
	v_cvt_f32_u32_e32 v10, v10
	v_rcp_iflag_f32_e32 v44, v10
	s_nop 0
	v_pk_mul_f32 v[10:11], v[44:45], s[2:3]
	s_nop 0
	v_mul_f32_e32 v14, 0x4b800000, v10
	v_pk_mul_f32 v[16:17], v[10:11], v[10:11] op_sel:[0,1] op_sel_hi:[1,0]
	s_nop 0
	v_fma_mixlo_f16 v15, v60, v14, v16
	v_pk_fma_f32 v[10:11], v[42:43], v[14:15], v[16:17] op_sel_hi:[1,0,0]
	v_pk_fma_f32 v[12:13], v[36:37], v[14:15], v[16:17] op_sel_hi:[1,0,0]
	v_pk_fma_f32 v[30:31], v[30:31], v[14:15], v[16:17] op_sel_hi:[1,0,0]
	v_cvt_pk_f16_f32 v11, v10, v11
	v_cvt_pk_f16_f32 v12, v12, v13
	v_cvt_pk_f16_f32 v13, v30, v31
	v_pack_b32_f16 v10, v15, v11
	v_alignbit_b32 v11, v12, v11, 16
	v_alignbit_b32 v12, v13, v12, 16
	v_lshrrev_b32_e32 v13, 16, v13
	v_fma_mixhi_f16 v13, v53, v14, v16
	v_add_u32_e32 v14, v18, v77
	v_xor_b32_e32 v15, v14, v0
	v_lshlrev_b32_e32 v15, 4, v15
	v_and_b32_e32 v15, 0xf0, v15
	v_lshl_or_b32 v14, v14, 8, v15
	ds_write_b128 v14, v[10:13]

.LBB2_43:
	s_lshl_b32 s28, s27, 2
	v_cmp_lt_i32_e32 vcc, s28, v5
	s_or_b32 s29, s28, 1
	s_add_i32 s27, s27, 1
	s_waitcnt lgkmcnt(0)
	v_cndmask_b32_e32 v11, v9, v80, vcc
	v_cmp_lt_i32_e32 vcc, s29, v5
	s_or_b32 s29, s28, 2
	s_or_b32 s28, s28, 3
	v_cndmask_b32_e32 v12, v9, v81, vcc
	v_cmp_lt_i32_e32 vcc, s29, v5
	v_lshl_or_b32 v14, v11, 7, v66
	v_lshlrev_b32_e32 v11, 2, v11
	v_cndmask_b32_e32 v13, v9, v82, vcc
	v_cmp_lt_i32_e32 vcc, s28, v5
	v_lshl_or_b32 v15, v12, 7, v66
	v_lshl_or_b32 v16, v13, 7, v66
	v_cndmask_b32_e32 v10, v9, v79, vcc
	v_lshl_or_b32 v17, v10, 7, v66
	global_load_dwordx2 v[38:39], v14, s[10:11]
	global_load_dwordx2 v[40:41], v15, s[10:11]
	global_load_dwordx2 v[32:33], v16, s[10:11]
	global_load_dwordx2 v[34:35], v17, s[10:11]
	v_lshlrev_b32_e32 v12, 2, v12
	v_lshlrev_b32_e32 v13, 2, v13
	v_lshlrev_b32_e32 v10, 2, v10
	global_load_dword v61, v11, s[12:13]
	global_load_dword v62, v12, s[12:13]
	global_load_dword v58, v13, s[12:13]
	global_load_dword v59, v10, s[12:13]
	s_cmp_lg_u32 s27, s21
	s_cbranch_scc1 .LBB2_49
	s_cmp_eq_u32 s20, 0
	s_cbranch_scc1 .LBB2_47
	s_add_i32 s27, s20, 1
	s_mov_b32 s20, 2
	s_cmp_eq_u32 s27, 2
	v_mov_b32_e32 v3, v7
	v_mov_b32_e32 v5, v51
	s_mov_b32 s21, s16
	s_cbranch_scc1 .LBB2_48
	s_cmp_eq_u32 s27, 3
	s_cselect_b64 vcc, -1, 0
	s_and_b64 s[20:21], vcc, exec
	v_cndmask_b32_e32 v5, 0, v52, vcc
	s_cselect_b32 s21, s6, 0x7fffffff
	s_mov_b32 s20, s27
	v_mov_b32_e32 v3, v8
	s_branch .LBB2_48

.LBB2_49:
	s_lshl_b32 s28, s27, 2
	v_add_u32_e32 v79, s28, v3
	v_lshl_add_u32 v79, v79, 2, v2
	ds_read_b32 v80, v79 offset:15360
	ds_read_b32 v81, v79 offset:15364
	ds_read_b32 v82, v79 offset:15368
	ds_read_b32 v79, v79 offset:15372
	s_waitcnt vmcnt(10)
	v_cvt_pk_f16_f32 v10, v56, v57
	v_perm_b32 v11, v28, v26, s23
	v_dot2c_f32_f16_e32 v60, v11, v10
	v_perm_b32 v11, v28, v26, s24
	v_dot2c_f32_f16_e32 v42, v11, v10
	v_perm_b32 v11, v28, v26, s25
	v_dot2c_f32_f16_e32 v43, v11, v10
	v_perm_b32 v11, v28, v26, s26
	v_dot2c_f32_f16_e32 v36, v11, v10
	v_perm_b32 v11, v29, v27, s23
	v_dot2c_f32_f16_e32 v37, v11, v10
	v_perm_b32 v11, v29, v27, s24
	v_dot2c_f32_f16_e32 v30, v11, v10
	v_perm_b32 v11, v29, v27, s25
	v_dot2c_f32_f16_e32 v31, v11, v10
	v_perm_b32 v11, v29, v27, s26
	v_dot2c_f32_f16_e32 v53, v11, v10
	v_dot2c_f32_f16_e32 v45, 0x3c003c00, v10
	s_waitcnt vmcnt(8)
	v_cvt_pk_f16_f32 v10, v54, v55
	v_perm_b32 v11, v24, v22, s23
	v_dot2c_f32_f16_e32 v60, v11, v10
	v_perm_b32 v11, v24, v22, s24
	v_dot2c_f32_f16_e32 v42, v11, v10
	v_perm_b32 v11, v24, v22, s25
	v_dot2c_f32_f16_e32 v43, v11, v10
	v_perm_b32 v11, v24, v22, s26
	v_dot2c_f32_f16_e32 v36, v11, v10
	v_perm_b32 v11, v25, v23, s23
	v_dot2c_f32_f16_e32 v37, v11, v10
	v_perm_b32 v11, v25, v23, s24
	v_dot2c_f32_f16_e32 v30, v11, v10
	v_perm_b32 v11, v25, v23, s25
	v_dot2c_f32_f16_e32 v31, v11, v10
	v_perm_b32 v11, v25, v23, s26
	s_add_i32 s5, s5, 1
	v_dot2c_f32_f16_e32 v53, v11, v10
	s_cmp_lg_u32 s5, s4
	v_dot2c_f32_f16_e32 v45, 0x3c003c00, v10
	s_cbranch_scc1 .LBB2_57
	v_cmp_gt_i32_e32 vcc, 15, v18
	s_and_saveexec_b64 s[4:5], vcc
	s_cbranch_execz .LBB2_52
	v_max_i32_e32 v10, 1, v44
	v_cvt_f32_u32_e32 v10, v10
	v_rcp_iflag_f32_e32 v44, v10
	s_nop 0
	v_pk_mul_f32 v[10:11], v[44:45], s[2:3]
	s_nop 0
	v_mul_f32_e32 v14, 0x4b800000, v10
	v_pk_mul_f32 v[16:17], v[10:11], v[10:11] op_sel:[0,1] op_sel_hi:[1,0]
	s_nop 0
	v_fma_mixlo_f16 v15, v60, v14, v16
	v_pk_fma_f32 v[10:11], v[42:43], v[14:15], v[16:17] op_sel_hi:[1,0,0]
	v_pk_fma_f32 v[12:13], v[36:37], v[14:15], v[16:17] op_sel_hi:[1,0,0]
	v_pk_fma_f32 v[22:23], v[30:31], v[14:15], v[16:17] op_sel_hi:[1,0,0]
	v_cvt_pk_f16_f32 v11, v10, v11
	v_cvt_pk_f16_f32 v12, v12, v13
	v_cvt_pk_f16_f32 v13, v22, v23
	v_pack_b32_f16 v10, v15, v11
	v_alignbit_b32 v11, v12, v11, 16
	v_alignbit_b32 v12, v13, v12, 16
	v_lshrrev_b32_e32 v13, 16, v13
	v_fma_mixhi_f16 v13, v53, v14, v16
	v_add_u32_e32 v14, v18, v77
	v_xor_b32_e32 v15, v14, v0
	v_lshlrev_b32_e32 v15, 4, v15
	v_and_b32_e32 v15, 0xf0, v15
	v_lshl_or_b32 v14, v14, 8, v15
	ds_write_b128 v14, v[10:13]

.LBB2_57:
	s_lshl_b32 s28, s27, 2
	v_cmp_lt_i32_e32 vcc, s28, v5
	s_or_b32 s29, s28, 1
	s_add_i32 s27, s27, 1
	s_waitcnt lgkmcnt(0)
	v_cndmask_b32_e32 v11, v9, v80, vcc
	v_cmp_lt_i32_e32 vcc, s29, v5
	s_or_b32 s29, s28, 2
	s_or_b32 s28, s28, 3
	v_cndmask_b32_e32 v12, v9, v81, vcc
	v_cmp_lt_i32_e32 vcc, s29, v5
	v_lshl_or_b32 v14, v11, 7, v66
	v_lshlrev_b32_e32 v11, 2, v11
	v_cndmask_b32_e32 v13, v9, v82, vcc
	v_cmp_lt_i32_e32 vcc, s28, v5
	v_lshl_or_b32 v15, v12, 7, v66
	v_lshl_or_b32 v16, v13, 7, v66
	v_cndmask_b32_e32 v10, v9, v79, vcc
	v_lshl_or_b32 v17, v10, 7, v66
	global_load_dwordx2 v[26:27], v14, s[10:11]
	global_load_dwordx2 v[28:29], v15, s[10:11]
	global_load_dwordx2 v[22:23], v16, s[10:11]
	global_load_dwordx2 v[24:25], v17, s[10:11]
	v_lshlrev_b32_e32 v12, 2, v12
	v_lshlrev_b32_e32 v13, 2, v13
	v_lshlrev_b32_e32 v10, 2, v10
	global_load_dword v56, v11, s[12:13]
	global_load_dword v57, v12, s[12:13]
	global_load_dword v54, v13, s[12:13]
	global_load_dword v55, v10, s[12:13]
	s_cmp_lg_u32 s27, s21
	s_cbranch_scc1 .LBB2_34
	s_cmp_eq_u32 s20, 0
	s_cbranch_scc1 .LBB2_32
	s_add_i32 s27, s20, 1
	s_mov_b32 s20, 2
	s_cmp_eq_u32 s27, 2
	v_mov_b32_e32 v3, v7
	v_mov_b32_e32 v5, v51
	s_mov_b32 s21, s16
	s_cbranch_scc1 .LBB2_33
	s_cmp_eq_u32 s27, 3
	s_cselect_b64 vcc, -1, 0
	s_and_b64 s[20:21], vcc, exec
	v_cndmask_b32_e32 v5, 0, v52, vcc
	s_cselect_b32 s21, s6, 0x7fffffff
	s_mov_b32 s20, s27
	v_mov_b32_e32 v3, v8
	s_branch .LBB2_33

.LBB2_71:
	s_or_b64 exec, exec, s[0:1]
	v_lshlrev_b32_e32 v14, 2, v72
	v_lshlrev_b32_e32 v10, 4, v73
	v_or_b32_e32 v12, v14, v1
	s_movk_i32 s8, 0x110
	v_mad_u32_u24 v2, v12, s8, v10
	s_waitcnt lgkmcnt(0)
	s_barrier
	ds_read_b128 v[2:5], v2
	v_mov_b32_e32 v67, 0
	v_mov_b32_e32 v11, v67
	v_lshl_add_u64 v[8:9], s[4:5], 0, v[10:11]
	v_add_u32_e32 v12, s18, v12
	s_waitcnt lgkmcnt(0)
	v_cvt_f32_f16_e32 v13, v2
	v_cvt_f32_f16_sdwa v15, v2 dst_sel:DWORD dst_unused:UNUSED_PAD src0_sel:WORD_1
	v_cvt_f32_f16_e32 v16, v3
	v_cvt_f32_f16_sdwa v17, v3 dst_sel:DWORD dst_unused:UNUSED_PAD src0_sel:WORD_1
	v_cvt_f32_f16_e32 v19, v4
	v_cvt_f32_f16_sdwa v20, v4 dst_sel:DWORD dst_unused:UNUSED_PAD src0_sel:WORD_1
	v_cvt_f32_f16_e32 v21, v5
	v_cvt_f32_f16_sdwa v22, v5 dst_sel:DWORD dst_unused:UNUSED_PAD src0_sel:WORD_1
	v_max3_f32 v11, v13, 0, v15
	v_max3_f32 v11, v11, v16, v17
	v_max3_f32 v11, v11, v19, v20
	v_max3_f32 v11, v11, v21, v22
	v_cmp_ne_u32_e64 s[0:1], 15, v72
	s_mov_b32 s4, 0x186a0
	v_mov_b32_dpp v18, v11 quad_perm:[1,0,3,2] row_mask:0xf bank_mask:0xf bound_ctrl:1
	v_max_f32_e32 v18, v18, v18
	v_max_f32_e32 v11, v11, v18
	v_lshl_add_u64 v[6:7], s[6:7], 0, v[66:67]
	v_cmp_eq_u32_e32 vcc, 0, v73
	v_mov_b32_dpp v18, v11 quad_perm:[2,3,0,1] row_mask:0xf bank_mask:0xf bound_ctrl:1
	v_max_f32_e32 v18, v18, v18
	v_max_f32_e32 v11, v11, v18
	s_nop 1
	v_mov_b32_dpp v18, v11 row_half_mirror row_mask:0xf bank_mask:0xf bound_ctrl:1
	v_max_f32_e32 v18, v18, v18
	v_max_f32_e32 v18, v11, v18
	v_mov_b32_e32 v11, 0x186a0
	v_cndmask_b32_e64 v12, v11, v12, s[0:1]
	v_mov_b32_dpp v23, v18 row_mirror row_mask:0xf bank_mask:0xf bound_ctrl:1
	v_cmp_gt_i32_e64 s[0:1], s4, v12
	s_and_saveexec_b64 s[2:3], s[0:1]
	s_cbranch_execz .LBB2_74
	v_max_f32_e32 v23, v23, v23
	v_max_f32_e32 v18, v18, v18
	v_max_f32_e32 v18, v18, v23
	v_rcp_f32_e32 v23, v18
	v_cmp_lt_f32_e64 s[0:1], 0, v18
	v_mul_f32_e32 v23, 0x437f0000, v23
	s_nop 0
	v_cndmask_b32_e64 v23, 0, v23, s[0:1]
	v_mul_f32_e32 v13, v23, v13
	v_mul_f32_e32 v19, v23, v19
	v_mul_f32_e32 v15, v23, v15
	v_rndne_f32_e32 v13, v13
	v_mul_f32_e32 v20, v23, v20
	v_rndne_f32_e32 v19, v19
	v_mul_f32_e32 v16, v23, v16
	v_rndne_f32_e32 v15, v15
	v_cvt_pk_u8_f32 v13, v13, 0, 0
	v_mul_f32_e32 v21, v23, v21
	v_rndne_f32_e32 v20, v20
	v_cvt_pk_u8_f32 v19, v19, 0, 0
	v_mul_f32_e32 v17, v23, v17
	v_rndne_f32_e32 v16, v16
	v_cvt_pk_u8_f32 v13, v15, 1, v13
	v_mul_f32_e32 v22, v23, v22
	v_rndne_f32_e32 v21, v21
	v_cvt_pk_u8_f32 v19, v20, 1, v19
	v_rndne_f32_e32 v17, v17
	v_cvt_pk_u8_f32 v13, v16, 2, v13
	v_rndne_f32_e32 v22, v22
	v_cvt_pk_u8_f32 v19, v21, 2, v19
	v_cvt_pk_u8_f32 v20, v17, 3, v13
	v_ashrrev_i32_e32 v13, 31, v12
	v_cvt_pk_u8_f32 v21, v22, 3, v19
	v_lshlrev_b64 v[22:23], 8, v[12:13]
	v_lshlrev_b64 v[16:17], 7, v[12:13]
	v_lshl_add_u64 v[22:23], v[8:9], 0, v[22:23]
	global_store_dwordx4 v[22:23], v[2:5], off sc1
	s_nop 1
	v_lshl_add_u64 v[2:3], v[6:7], 0, v[16:17]
	global_store_dwordx2 v[2:3], v[20:21], off sc1
	s_and_b64 exec, exec, vcc
	s_cbranch_execz .LBB2_74
	v_lshl_add_u64 v[2:3], v[12:13], 2, s[14:15]
	v_mul_f32_e32 v4, 0x40808081, v18
	global_store_dword v[2:3], v4, off
.LBB2_74:
	s_or_b64 exec, exec, s[2:3]
	v_add3_u32 v12, v14, v1, 16
	v_mad_u32_u24 v2, v12, s8, v10
	ds_read_b128 v[2:5], v2
	s_movk_i32 s0, 0x2c0
	v_add_u32_e32 v12, s18, v12
	v_cmp_gt_u32_e64 s[0:1], s0, v0
	s_waitcnt lgkmcnt(0)
	v_cvt_f32_f16_e32 v13, v2
	v_cvt_f32_f16_sdwa v15, v2 dst_sel:DWORD dst_unused:UNUSED_PAD src0_sel:WORD_1
	v_cvt_f32_f16_e32 v16, v3
	v_cvt_f32_f16_sdwa v17, v3 dst_sel:DWORD dst_unused:UNUSED_PAD src0_sel:WORD_1
	v_cvt_f32_f16_e32 v18, v4
	v_cvt_f32_f16_sdwa v19, v4 dst_sel:DWORD dst_unused:UNUSED_PAD src0_sel:WORD_1
	v_cvt_f32_f16_e32 v20, v5
	v_cvt_f32_f16_sdwa v21, v5 dst_sel:DWORD dst_unused:UNUSED_PAD src0_sel:WORD_1
	v_max3_f32 v22, v13, 0, v15
	v_max3_f32 v22, v22, v16, v17
	v_max3_f32 v22, v22, v18, v19
	v_max3_f32 v22, v22, v20, v21
	v_cndmask_b32_e64 v12, v11, v12, s[0:1]
	v_cmp_gt_i32_e64 s[0:1], s4, v12
	v_mov_b32_dpp v23, v22 quad_perm:[1,0,3,2] row_mask:0xf bank_mask:0xf bound_ctrl:1
	v_max_f32_e32 v23, v23, v23
	v_max_f32_e32 v22, v22, v23
	s_nop 1
	v_mov_b32_dpp v23, v22 quad_perm:[2,3,0,1] row_mask:0xf bank_mask:0xf bound_ctrl:1
	v_max_f32_e32 v23, v23, v23
	v_max_f32_e32 v22, v22, v23
	s_nop 1
	v_mov_b32_dpp v23, v22 row_half_mirror row_mask:0xf bank_mask:0xf bound_ctrl:1
	v_max_f32_e32 v23, v23, v23
	v_max_f32_e32 v22, v22, v23
	s_nop 1
	v_mov_b32_dpp v23, v22 row_mirror row_mask:0xf bank_mask:0xf bound_ctrl:1
	s_and_saveexec_b64 s[2:3], s[0:1]
	s_cbranch_execz .LBB2_77
	v_max_f32_e32 v11, v23, v23
	v_max_f32_e32 v22, v22, v22
	v_max_f32_e32 v11, v22, v11
	v_rcp_f32_e32 v22, v11
	v_cmp_lt_f32_e64 s[0:1], 0, v11
	v_mul_f32_e32 v22, 0x437f0000, v22
	s_nop 0
	v_cndmask_b32_e64 v22, 0, v22, s[0:1]
	v_mul_f32_e32 v18, v22, v18
	v_mul_f32_e32 v13, v22, v13
	v_mul_f32_e32 v19, v22, v19
	v_rndne_f32_e32 v18, v18
	v_mul_f32_e32 v15, v22, v15
	v_rndne_f32_e32 v13, v13
	v_mul_f32_e32 v20, v22, v20
	v_rndne_f32_e32 v19, v19
	v_cvt_pk_u8_f32 v18, v18, 0, 0
	v_mul_f32_e32 v16, v22, v16
	v_rndne_f32_e32 v15, v15
	v_cvt_pk_u8_f32 v13, v13, 0, 0
	v_mul_f32_e32 v21, v22, v21
	v_rndne_f32_e32 v20, v20
	v_cvt_pk_u8_f32 v18, v19, 1, v18
	v_mul_f32_e32 v17, v22, v17
	v_rndne_f32_e32 v16, v16
	v_cvt_pk_u8_f32 v13, v15, 1, v13
	v_rndne_f32_e32 v21, v21
	v_cvt_pk_u8_f32 v18, v20, 2, v18
	v_rndne_f32_e32 v17, v17
	v_cvt_pk_u8_f32 v13, v16, 2, v13
	v_cvt_pk_u8_f32 v19, v21, 3, v18
	v_cvt_pk_u8_f32 v18, v17, 3, v13
	v_ashrrev_i32_e32 v13, 31, v12
	v_lshlrev_b64 v[20:21], 8, v[12:13]
	v_lshlrev_b64 v[16:17], 7, v[12:13]
	v_lshl_add_u64 v[20:21], v[8:9], 0, v[20:21]
	global_store_dwordx4 v[20:21], v[2:5], off sc1
	s_nop 1
	v_lshl_add_u64 v[2:3], v[6:7], 0, v[16:17]
	global_store_dwordx2 v[2:3], v[18:19], off sc1
	s_and_b64 exec, exec, vcc
	s_cbranch_execz .LBB2_77
	v_lshl_add_u64 v[2:3], v[12:13], 2, s[14:15]
	v_mul_f32_e32 v4, 0x40808081, v11
	global_store_dword v[2:3], v4, off
.LBB2_77:
	s_or_b64 exec, exec, s[2:3]
	v_add_u32_e32 v2, v14, v1
	v_or_b32_e32 v11, 32, v2
	s_movk_i32 s5, 0x110
	v_mad_u32_u24 v2, v11, s5, v10
	ds_read_b128 v[2:5], v2
	v_add_u32_e32 v12, s18, v11
	s_movk_i32 s0, 0x1c0
	v_cmp_gt_u32_e64 s[0:1], s0, v0
	s_waitcnt lgkmcnt(0)
	v_cvt_f32_f16_e32 v13, v2
	v_cvt_f32_f16_sdwa v15, v2 dst_sel:DWORD dst_unused:UNUSED_PAD src0_sel:WORD_1
	v_cvt_f32_f16_e32 v16, v3
	v_cvt_f32_f16_sdwa v17, v3 dst_sel:DWORD dst_unused:UNUSED_PAD src0_sel:WORD_1
	v_cvt_f32_f16_e32 v19, v4
	v_cvt_f32_f16_sdwa v20, v4 dst_sel:DWORD dst_unused:UNUSED_PAD src0_sel:WORD_1
	v_cvt_f32_f16_e32 v21, v5
	v_cvt_f32_f16_sdwa v22, v5 dst_sel:DWORD dst_unused:UNUSED_PAD src0_sel:WORD_1
	v_max3_f32 v11, v13, 0, v15
	v_max3_f32 v11, v11, v16, v17
	v_max3_f32 v11, v11, v19, v20
	v_max3_f32 v11, v11, v21, v22
	s_nop 1
	v_mov_b32_dpp v18, v11 quad_perm:[1,0,3,2] row_mask:0xf bank_mask:0xf bound_ctrl:1
	v_max_f32_e32 v18, v18, v18
	v_max_f32_e32 v11, v11, v18
	s_nop 1
	v_mov_b32_dpp v18, v11 quad_perm:[2,3,0,1] row_mask:0xf bank_mask:0xf bound_ctrl:1
	v_max_f32_e32 v18, v18, v18
	v_max_f32_e32 v11, v11, v18
	s_nop 1
	v_mov_b32_dpp v18, v11 row_half_mirror row_mask:0xf bank_mask:0xf bound_ctrl:1
	v_max_f32_e32 v18, v18, v18
	v_max_f32_e32 v18, v11, v18
	v_mov_b32_e32 v11, 0x186a0
	v_cndmask_b32_e64 v12, v11, v12, s[0:1]
	v_mov_b32_dpp v23, v18 row_mirror row_mask:0xf bank_mask:0xf bound_ctrl:1
	v_cmp_gt_i32_e64 s[0:1], s4, v12
	s_and_saveexec_b64 s[2:3], s[0:1]
	s_cbranch_execz .LBB2_80
	v_max_f32_e32 v23, v23, v23
	v_max_f32_e32 v18, v18, v18
	v_max_f32_e32 v18, v18, v23
	v_rcp_f32_e32 v23, v18
	v_cmp_lt_f32_e64 s[0:1], 0, v18
	v_mul_f32_e32 v23, 0x437f0000, v23
	s_nop 0
	v_cndmask_b32_e64 v23, 0, v23, s[0:1]
	v_mul_f32_e32 v13, v23, v13
	v_mul_f32_e32 v19, v23, v19
	v_mul_f32_e32 v15, v23, v15
	v_rndne_f32_e32 v13, v13
	v_mul_f32_e32 v20, v23, v20
	v_rndne_f32_e32 v19, v19
	v_mul_f32_e32 v16, v23, v16
	v_rndne_f32_e32 v15, v15
	v_cvt_pk_u8_f32 v13, v13, 0, 0
	v_mul_f32_e32 v21, v23, v21
	v_rndne_f32_e32 v20, v20
	v_cvt_pk_u8_f32 v19, v19, 0, 0
	v_mul_f32_e32 v17, v23, v17
	v_rndne_f32_e32 v16, v16
	v_cvt_pk_u8_f32 v13, v15, 1, v13
	v_mul_f32_e32 v22, v23, v22
	v_rndne_f32_e32 v21, v21
	v_cvt_pk_u8_f32 v19, v20, 1, v19
	v_rndne_f32_e32 v17, v17
	v_cvt_pk_u8_f32 v13, v16, 2, v13
	v_rndne_f32_e32 v22, v22
	v_cvt_pk_u8_f32 v19, v21, 2, v19
	v_cvt_pk_u8_f32 v20, v17, 3, v13
	v_ashrrev_i32_e32 v13, 31, v12
	v_cvt_pk_u8_f32 v21, v22, 3, v19
	v_lshlrev_b64 v[22:23], 8, v[12:13]
	v_lshlrev_b64 v[16:17], 7, v[12:13]
	v_lshl_add_u64 v[22:23], v[8:9], 0, v[22:23]
	global_store_dwordx4 v[22:23], v[2:5], off sc1
	s_nop 1
	v_lshl_add_u64 v[2:3], v[6:7], 0, v[16:17]
	global_store_dwordx2 v[2:3], v[20:21], off sc1
	s_and_b64 exec, exec, vcc
	s_cbranch_execz .LBB2_80
	v_lshl_add_u64 v[2:3], v[12:13], 2, s[14:15]
	v_mul_f32_e32 v4, 0x40808081, v18
	global_store_dword v[2:3], v4, off
.LBB2_80:
	s_or_b64 exec, exec, s[2:3]
	v_add3_u32 v1, v14, v1, 48
	v_min_i32_e32 v2, 59, v1
	v_mad_u32_u24 v2, v2, s5, v10
	ds_read_b128 v[2:5], v2
	v_add_u32_e32 v20, s18, v1
	s_movk_i32 s0, 0xc0
	v_cmp_gt_u32_e64 s[0:1], s0, v0
	s_waitcnt lgkmcnt(0)
	v_cvt_f32_f16_e32 v1, v2
	v_cvt_f32_f16_sdwa v10, v2 dst_sel:DWORD dst_unused:UNUSED_PAD src0_sel:WORD_1
	v_cvt_f32_f16_e32 v12, v3
	v_cvt_f32_f16_sdwa v13, v3 dst_sel:DWORD dst_unused:UNUSED_PAD src0_sel:WORD_1
	v_cvt_f32_f16_e32 v14, v4
	v_cvt_f32_f16_sdwa v15, v4 dst_sel:DWORD dst_unused:UNUSED_PAD src0_sel:WORD_1
	v_cvt_f32_f16_e32 v16, v5
	v_cvt_f32_f16_sdwa v17, v5 dst_sel:DWORD dst_unused:UNUSED_PAD src0_sel:WORD_1
	v_max3_f32 v18, v1, 0, v10
	v_max3_f32 v18, v18, v12, v13
	v_max3_f32 v18, v18, v14, v15
	v_max3_f32 v18, v18, v16, v17
	v_cndmask_b32_e64 v0, v11, v20, s[0:1]
	v_cmp_gt_i32_e64 s[0:1], s4, v0
	v_mov_b32_dpp v19, v18 quad_perm:[1,0,3,2] row_mask:0xf bank_mask:0xf bound_ctrl:1
	v_max_f32_e32 v19, v19, v19
	v_max_f32_e32 v18, v18, v19
	s_nop 1
	v_mov_b32_dpp v19, v18 quad_perm:[2,3,0,1] row_mask:0xf bank_mask:0xf bound_ctrl:1
	v_max_f32_e32 v19, v19, v19
	v_max_f32_e32 v18, v18, v19
	s_nop 1
	v_mov_b32_dpp v19, v18 row_half_mirror row_mask:0xf bank_mask:0xf bound_ctrl:1
	v_max_f32_e32 v19, v19, v19
	v_max_f32_e32 v18, v18, v19
	s_nop 1
	v_mov_b32_dpp v19, v18 row_mirror row_mask:0xf bank_mask:0xf bound_ctrl:1
	s_and_saveexec_b64 s[2:3], s[0:1]
	s_cbranch_execz .LBB2_83
	v_max_f32_e32 v11, v19, v19
	v_max_f32_e32 v18, v18, v18
	v_max_f32_e32 v11, v18, v11
	v_rcp_f32_e32 v18, v11
	v_cmp_lt_f32_e64 s[0:1], 0, v11
	v_mul_f32_e32 v18, 0x437f0000, v18
	s_nop 0
	v_cndmask_b32_e64 v18, 0, v18, s[0:1]
	v_mul_f32_e32 v14, v18, v14
	v_mul_f32_e32 v1, v18, v1
	v_mul_f32_e32 v15, v18, v15
	v_rndne_f32_e32 v14, v14
	v_mul_f32_e32 v10, v18, v10
	v_rndne_f32_e32 v1, v1
	v_mul_f32_e32 v16, v18, v16
	v_rndne_f32_e32 v15, v15
	v_cvt_pk_u8_f32 v14, v14, 0, 0
	v_mul_f32_e32 v12, v18, v12
	v_rndne_f32_e32 v10, v10
	v_cvt_pk_u8_f32 v1, v1, 0, 0
	v_mul_f32_e32 v17, v18, v17
	v_rndne_f32_e32 v16, v16
	v_cvt_pk_u8_f32 v14, v15, 1, v14
	v_mul_f32_e32 v13, v18, v13
	v_rndne_f32_e32 v12, v12
	v_cvt_pk_u8_f32 v1, v10, 1, v1
	v_rndne_f32_e32 v17, v17
	v_cvt_pk_u8_f32 v14, v16, 2, v14
	v_rndne_f32_e32 v13, v13
	v_cvt_pk_u8_f32 v1, v12, 2, v1
	v_cvt_pk_u8_f32 v15, v17, 3, v14
	v_cvt_pk_u8_f32 v14, v13, 3, v1
	v_ashrrev_i32_e32 v1, 31, v0
	v_lshlrev_b64 v[16:17], 8, v[0:1]
	v_lshlrev_b64 v[12:13], 7, v[0:1]
	v_lshl_add_u64 v[8:9], v[8:9], 0, v[16:17]
	global_store_dwordx4 v[8:9], v[2:5], off sc1
	s_nop 1
	v_lshl_add_u64 v[2:3], v[6:7], 0, v[12:13]
	global_store_dwordx2 v[2:3], v[14:15], off sc1
	s_and_b64 exec, exec, vcc
	s_cbranch_execz .LBB2_83
	v_lshl_add_u64 v[0:1], v[0:1], 2, s[14:15]
	v_mul_f32_e32 v2, 0x40808081, v11
	global_store_dword v[0:1], v2, off

.LBB2_107:
	s_or_b64 exec, exec, s[2:3]
	s_load_dwordx4 s[4:7], s[0:1], 0x38
	s_cmpk_lt_i32 s19, 0x181
	s_cbranch_scc0 .LBB2_62
	s_branch .LBB2_63
	s_nop 0
	s_nop 0
	s_nop 0
	s_nop 0
	s_nop 0
	s_nop 0
	s_nop 0
	s_nop 0
	s_nop 0
	s_nop 0
	s_endpgm

.LBB3_33:
	s_lshl_b32 s26, s25, 2
	v_add_u32_e32 v82, s26, v3
	v_lshl_add_u32 v82, v82, 2, v2
	ds_read_b32 v83, v82 offset:15360
	ds_read_b32 v84, v82 offset:15364
	ds_read_b32 v85, v82 offset:15368
	ds_read_b32 v82, v82 offset:15372
	s_waitcnt vmcnt(10)
	v_cvt_pk_f16_f32 v9, v57, v58
	v_perm_b32 v10, v40, v38, s21
	v_dot2c_f32_f16_e32 v56, v10, v9
	v_perm_b32 v10, v40, v38, s22
	v_dot2c_f32_f16_e32 v42, v10, v9
	v_perm_b32 v10, v40, v38, s23
	v_dot2c_f32_f16_e32 v43, v10, v9
	v_perm_b32 v10, v40, v38, s24
	v_dot2c_f32_f16_e32 v36, v10, v9
	v_perm_b32 v10, v41, v39, s21
	v_dot2c_f32_f16_e32 v37, v10, v9
	v_perm_b32 v10, v41, v39, s22
	v_dot2c_f32_f16_e32 v30, v10, v9
	v_perm_b32 v10, v41, v39, s23
	v_dot2c_f32_f16_e32 v31, v10, v9
	v_perm_b32 v10, v41, v39, s24
	v_dot2c_f32_f16_e32 v49, v10, v9
	s_waitcnt vmcnt(8)
	v_cvt_pk_f16_f32 v9, v54, v55
	v_perm_b32 v10, v34, v32, s21
	v_dot2c_f32_f16_e32 v56, v10, v9
	v_perm_b32 v10, v34, v32, s22
	v_dot2c_f32_f16_e32 v42, v10, v9
	v_perm_b32 v10, v34, v32, s23
	v_dot2c_f32_f16_e32 v43, v10, v9
	v_perm_b32 v10, v34, v32, s24
	v_dot2c_f32_f16_e32 v36, v10, v9
	v_perm_b32 v10, v35, v33, s21
	v_dot2c_f32_f16_e32 v37, v10, v9
	v_perm_b32 v10, v35, v33, s22
	v_dot2c_f32_f16_e32 v30, v10, v9
	v_perm_b32 v10, v35, v33, s23
	v_dot2c_f32_f16_e32 v31, v10, v9
	v_perm_b32 v10, v35, v33, s24
	s_add_i32 s5, s5, 1
	v_dot2c_f32_f16_e32 v49, v10, v9
	s_cmp_lg_u32 s5, s4
	s_cbranch_scc1 .LBB3_41
	v_cmp_gt_i32_e32 vcc, 15, v18
	s_and_saveexec_b64 s[4:5], vcc
	s_cbranch_execz .LBB3_36
	v_max_i32_e32 v9, 1, v44
	v_cvt_f32_u32_e32 v9, v9
	v_rcp_iflag_f32_e32 v44, v9
	s_nop 0
	v_pk_mul_f32 v[10:11], v[44:45], s[2:3]
	s_nop 0
	v_mul_f32_e32 v14, 0x4b800000, v10
	v_pk_mul_f32 v[16:17], v[10:11], v[10:11] op_sel:[0,1] op_sel_hi:[1,0]
	s_nop 0
	v_pk_fma_f32 v[10:11], v[42:43], v[14:15], v[16:17] op_sel_hi:[1,0,0]
	v_fma_mixlo_f16 v9, v56, v14, v16
	v_pk_fma_f32 v[12:13], v[36:37], v[14:15], v[16:17] op_sel_hi:[1,0,0]
	v_pk_fma_f32 v[30:31], v[30:31], v[14:15], v[16:17] op_sel_hi:[1,0,0]
	v_cvt_pk_f16_f32 v11, v10, v11
	v_cvt_pk_f16_f32 v12, v12, v13
	v_pack_b32_f16 v10, v9, v11
	v_cvt_pk_f16_f32 v9, v30, v31
	v_alignbit_b32 v11, v12, v11, 16
	v_alignbit_b32 v12, v9, v12, 16
	v_lshrrev_b32_e32 v13, 16, v9
	v_add_u32_e32 v9, v18, v75
	v_fma_mixhi_f16 v13, v49, v14, v16
	v_xor_b32_e32 v14, v9, v0
	v_lshlrev_b32_e32 v14, 4, v14
	v_and_b32_e32 v14, 0xf0, v14
	v_lshl_or_b32 v9, v9, 8, v14
	ds_write_b128 v9, v[10:13]

.LBB3_41:
	s_lshl_b32 s26, s25, 2
	v_cmp_lt_i32_e32 vcc, s26, v5
	s_or_b32 s27, s26, 1
	s_add_i32 s25, s25, 1
	s_waitcnt lgkmcnt(0)
	v_cndmask_b32_e32 v10, v8, v83, vcc
	v_cmp_lt_i32_e32 vcc, s27, v5
	s_or_b32 s27, s26, 2
	s_or_b32 s26, s26, 3
	v_cndmask_b32_e32 v11, v8, v84, vcc
	v_cmp_lt_i32_e32 vcc, s27, v5
	v_lshl_or_b32 v13, v10, 7, v78
	v_lshlrev_b32_e32 v10, 2, v10
	v_cndmask_b32_e32 v12, v8, v85, vcc
	v_cmp_lt_i32_e32 vcc, s26, v5
	v_lshl_or_b32 v14, v11, 7, v78
	v_lshl_or_b32 v15, v12, 7, v78
	v_cndmask_b32_e32 v9, v8, v82, vcc
	v_lshl_or_b32 v16, v9, 7, v78
	global_load_dwordx2 v[38:39], v13, s[10:11]
	global_load_dwordx2 v[40:41], v14, s[10:11]
	global_load_dwordx2 v[32:33], v15, s[10:11]
	global_load_dwordx2 v[34:35], v16, s[10:11]
	v_lshlrev_b32_e32 v11, 2, v11
	v_lshlrev_b32_e32 v12, 2, v12
	v_lshlrev_b32_e32 v9, 2, v9
	global_load_dword v57, v10, s[12:13]
	global_load_dword v58, v11, s[12:13]
	global_load_dword v54, v12, s[12:13]
	global_load_dword v55, v9, s[12:13]
	s_cmp_lg_u32 s25, s19
	s_cbranch_scc1 .LBB3_47
	s_cmp_eq_u32 s7, 0
	s_cbranch_scc1 .LBB3_45
	s_add_i32 s25, s7, 1
	s_mov_b32 s7, 2
	s_cmp_eq_u32 s25, 2
	v_mov_b32_e32 v3, v6
	v_mov_b32_e32 v5, v47
	s_mov_b32 s19, s15
	s_cbranch_scc1 .LBB3_46
	s_cmp_eq_u32 s25, 3
	s_cselect_b64 vcc, -1, 0
	s_and_b64 s[26:27], vcc, exec
	v_cndmask_b32_e32 v5, 0, v48, vcc
	s_cselect_b32 s19, s6, 0x7fffffff
	s_mov_b32 s7, s25
	v_mov_b32_e32 v3, v7
	s_branch .LBB3_46

.LBB3_47:
	s_lshl_b32 s26, s25, 2
	v_add_u32_e32 v82, s26, v3
	v_lshl_add_u32 v82, v82, 2, v2
	ds_read_b32 v83, v82 offset:15360
	ds_read_b32 v84, v82 offset:15364
	ds_read_b32 v85, v82 offset:15368
	ds_read_b32 v82, v82 offset:15372
	s_waitcnt vmcnt(10)
	v_cvt_pk_f16_f32 v9, v52, v53
	v_perm_b32 v10, v28, v26, s21
	v_dot2c_f32_f16_e32 v56, v10, v9
	v_perm_b32 v10, v28, v26, s22
	v_dot2c_f32_f16_e32 v42, v10, v9
	v_perm_b32 v10, v28, v26, s23
	v_dot2c_f32_f16_e32 v43, v10, v9
	v_perm_b32 v10, v28, v26, s24
	v_dot2c_f32_f16_e32 v36, v10, v9
	v_perm_b32 v10, v29, v27, s21
	v_dot2c_f32_f16_e32 v37, v10, v9
	v_perm_b32 v10, v29, v27, s22
	v_dot2c_f32_f16_e32 v30, v10, v9
	v_perm_b32 v10, v29, v27, s23
	v_dot2c_f32_f16_e32 v31, v10, v9
	v_perm_b32 v10, v29, v27, s24
	v_dot2c_f32_f16_e32 v49, v10, v9
	s_waitcnt vmcnt(8)
	v_cvt_pk_f16_f32 v9, v50, v51
	v_perm_b32 v10, v24, v22, s21
	v_dot2c_f32_f16_e32 v56, v10, v9
	v_perm_b32 v10, v24, v22, s22
	v_dot2c_f32_f16_e32 v42, v10, v9
	v_perm_b32 v10, v24, v22, s23
	v_dot2c_f32_f16_e32 v43, v10, v9
	v_perm_b32 v10, v24, v22, s24
	v_dot2c_f32_f16_e32 v36, v10, v9
	v_perm_b32 v10, v25, v23, s21
	v_dot2c_f32_f16_e32 v37, v10, v9
	v_perm_b32 v10, v25, v23, s22
	v_dot2c_f32_f16_e32 v30, v10, v9
	v_perm_b32 v10, v25, v23, s23
	v_dot2c_f32_f16_e32 v31, v10, v9
	v_perm_b32 v10, v25, v23, s24
	s_add_i32 s5, s5, 1
	v_dot2c_f32_f16_e32 v49, v10, v9
	s_cmp_lg_u32 s5, s4
	s_cbranch_scc1 .LBB3_55
	v_cmp_gt_i32_e32 vcc, 15, v18
	s_and_saveexec_b64 s[4:5], vcc
	s_cbranch_execz .LBB3_50
	v_max_i32_e32 v9, 1, v44
	v_cvt_f32_u32_e32 v9, v9
	v_rcp_iflag_f32_e32 v44, v9
	s_nop 0
	v_pk_mul_f32 v[10:11], v[44:45], s[2:3]
	s_nop 0
	v_mul_f32_e32 v14, 0x4b800000, v10
	v_pk_mul_f32 v[16:17], v[10:11], v[10:11] op_sel:[0,1] op_sel_hi:[1,0]
	s_nop 0
	v_pk_fma_f32 v[10:11], v[42:43], v[14:15], v[16:17] op_sel_hi:[1,0,0]
	v_fma_mixlo_f16 v9, v56, v14, v16
	v_pk_fma_f32 v[12:13], v[36:37], v[14:15], v[16:17] op_sel_hi:[1,0,0]
	v_pk_fma_f32 v[22:23], v[30:31], v[14:15], v[16:17] op_sel_hi:[1,0,0]
	v_cvt_pk_f16_f32 v11, v10, v11
	v_cvt_pk_f16_f32 v12, v12, v13
	v_pack_b32_f16 v10, v9, v11
	v_cvt_pk_f16_f32 v9, v22, v23
	v_alignbit_b32 v11, v12, v11, 16
	v_alignbit_b32 v12, v9, v12, 16
	v_lshrrev_b32_e32 v13, 16, v9
	v_add_u32_e32 v9, v18, v75
	v_fma_mixhi_f16 v13, v49, v14, v16
	v_xor_b32_e32 v14, v9, v0
	v_lshlrev_b32_e32 v14, 4, v14
	v_and_b32_e32 v14, 0xf0, v14
	v_lshl_or_b32 v9, v9, 8, v14
	ds_write_b128 v9, v[10:13]

.LBB3_55:
	s_lshl_b32 s26, s25, 2
	v_cmp_lt_i32_e32 vcc, s26, v5
	s_or_b32 s27, s26, 1
	s_add_i32 s25, s25, 1
	s_waitcnt lgkmcnt(0)
	v_cndmask_b32_e32 v10, v8, v83, vcc
	v_cmp_lt_i32_e32 vcc, s27, v5
	s_or_b32 s27, s26, 2
	s_or_b32 s26, s26, 3
	v_cndmask_b32_e32 v11, v8, v84, vcc
	v_cmp_lt_i32_e32 vcc, s27, v5
	v_lshl_or_b32 v13, v10, 7, v78
	v_lshlrev_b32_e32 v10, 2, v10
	v_cndmask_b32_e32 v12, v8, v85, vcc
	v_cmp_lt_i32_e32 vcc, s26, v5
	v_lshl_or_b32 v14, v11, 7, v78
	v_lshl_or_b32 v15, v12, 7, v78
	v_cndmask_b32_e32 v9, v8, v82, vcc
	v_lshl_or_b32 v16, v9, 7, v78
	global_load_dwordx2 v[26:27], v13, s[10:11]
	global_load_dwordx2 v[28:29], v14, s[10:11]
	global_load_dwordx2 v[22:23], v15, s[10:11]
	global_load_dwordx2 v[24:25], v16, s[10:11]
	v_lshlrev_b32_e32 v11, 2, v11
	v_lshlrev_b32_e32 v12, 2, v12
	v_lshlrev_b32_e32 v9, 2, v9
	global_load_dword v52, v10, s[12:13]
	global_load_dword v53, v11, s[12:13]
	global_load_dword v50, v12, s[12:13]
	global_load_dword v51, v9, s[12:13]
	s_cmp_lg_u32 s25, s19
	s_cbranch_scc1 .LBB3_32
	s_cmp_eq_u32 s7, 0
	s_cbranch_scc1 .LBB3_30
	s_add_i32 s25, s7, 1
	s_mov_b32 s7, 2
	s_cmp_eq_u32 s25, 2
	v_mov_b32_e32 v3, v6
	v_mov_b32_e32 v5, v47
	s_mov_b32 s19, s15
	s_cbranch_scc1 .LBB3_31
	s_cmp_eq_u32 s25, 3
	s_cselect_b64 vcc, -1, 0
	s_and_b64 s[26:27], vcc, exec
	v_cndmask_b32_e32 v5, 0, v48, vcc
	s_cselect_b32 s19, s6, 0x7fffffff
	s_mov_b32 s7, s25
	v_mov_b32_e32 v3, v7
	s_branch .LBB3_31

.LBB3_61:
	v_lshrrev_b32_e32 v67, 5, v66
	v_lshlrev_b32_e32 v88, 8, v72
	s_waitcnt vmcnt(8)
	v_xor_b32_e32 v2, v67, v71
	v_lshl_or_b32 v80, v2, 4, v88
	s_waitcnt lgkmcnt(0)
	s_barrier
	ds_read_b128 v[2:5], v80
	v_or_b32_e32 v6, 32, v72
	v_min_i32_e32 v72, 59, v6
	v_lshlrev_b32_e32 v89, 8, v72
	v_bitop3_b32 v6, v67, v72, 15 bitop3:0x78
	v_lshl_or_b32 v81, v6, 4, v89
	s_waitcnt vmcnt(7) lgkmcnt(0)
	v_mfma_f32_32x32x16_f16 v[18:33], v[2:5], v[46:49], 0
	ds_read_b128 v[2:5], v81
	v_and_b32_e32 v90, 15, v72
	v_bitop3_b32 v72, v67, v90, 2 bitop3:0x36
	v_lshl_or_b32 v79, v72, 4, v89
	s_mov_b32 s0, 0x9000
	s_waitcnt lgkmcnt(0)
	v_mfma_f32_32x32x16_f16 v[2:17], v[2:5], v[46:49], 0
	v_bitop3_b32 v46, v67, v71, 2 bitop3:0x36
	v_lshl_or_b32 v78, v46, 4, v88
	ds_read_b128 v[46:49], v78
	s_waitcnt vmcnt(6) lgkmcnt(0)
	v_mfma_f32_32x32x16_f16 v[18:33], v[46:49], v[34:37], v[18:33]
	ds_read_b128 v[46:49], v79
	s_waitcnt lgkmcnt(0)
	v_mfma_f32_32x32x16_f16 v[2:17], v[46:49], v[34:37], v[2:17]
	v_bitop3_b32 v34, v67, v71, 4 bitop3:0x36
	v_lshl_or_b32 v77, v34, 4, v88
	ds_read_b128 v[34:37], v77
	v_bitop3_b32 v46, v67, v90, 4 bitop3:0x36
	v_lshl_or_b32 v76, v46, 4, v89
	v_bitop3_b32 v46, v67, v90, 6 bitop3:0x36
	v_lshl_or_b32 v75, v46, 4, v89
	s_waitcnt vmcnt(5) lgkmcnt(0)
	v_mfma_f32_32x32x16_f16 v[18:33], v[34:37], v[54:57], v[18:33]
	ds_read_b128 v[34:37], v76
	v_bitop3_b32 v46, v67, v71, 8 bitop3:0x36
	v_lshl_or_b32 v72, v46, 4, v88
	s_waitcnt lgkmcnt(0)
	v_mfma_f32_32x32x16_f16 v[2:17], v[34:37], v[54:57], v[2:17]
	v_bitop3_b32 v34, v67, v71, 6 bitop3:0x36
	v_lshl_or_b32 v74, v34, 4, v88
	ds_read_b128 v[34:37], v74
	ds_read_b128 v[54:57], v72
	s_waitcnt vmcnt(4) lgkmcnt(1)
	v_mfma_f32_32x32x16_f16 v[18:33], v[34:37], v[38:41], v[18:33]
	ds_read_b128 v[34:37], v75
	s_waitcnt lgkmcnt(0)
	v_mfma_f32_32x32x16_f16 v[2:17], v[34:37], v[38:41], v[2:17]
	v_bitop3_b32 v34, v67, v90, 8 bitop3:0x36
	v_lshl_or_b32 v73, v34, 4, v89
	ds_read_b128 v[34:37], v73
	v_add_co_u32_e32 v38, vcc, s0, v68
	s_mov_b32 s0, 0xb000
	s_nop 0
	v_addc_co_u32_e32 v39, vcc, 0, v69, vcc
	s_waitcnt vmcnt(3) lgkmcnt(0)
	v_mfma_f32_32x32x16_f16 v[2:17], v[34:37], v[58:61], v[2:17]
	v_bitop3_b32 v34, v67, v71, 10 bitop3:0x36
	global_load_dwordx4 v[46:49], v[38:39], off offset:-4096
	v_add_co_u32_e32 v86, vcc, s0, v68
	s_mov_b32 s0, 0xd000
	s_nop 0
	v_addc_co_u32_e32 v87, vcc, 0, v69, vcc
	v_mfma_f32_32x32x16_f16 v[18:33], v[54:57], v[58:61], v[18:33]
	v_lshl_or_b32 v58, v34, 4, v88
	ds_read_b128 v[34:37], v58
	v_bitop3_b32 v54, v67, v90, 10 bitop3:0x36
	v_lshl_or_b32 v59, v54, 4, v89
	v_bitop3_b32 v54, v67, v71, 12 bitop3:0x36
	v_lshl_or_b32 v56, v54, 4, v88
	ds_read_b128 v[82:85], v56
	s_waitcnt vmcnt(3) lgkmcnt(1)
	v_mfma_f32_32x32x16_f16 v[18:33], v[34:37], v[42:45], v[18:33]
	ds_read_b128 v[34:37], v59
	v_bitop3_b32 v54, v67, v90, 14 bitop3:0x36
	v_lshl_or_b32 v54, v54, 4, v89
	s_waitcnt lgkmcnt(0)
	v_mfma_f32_32x32x16_f16 v[2:17], v[34:37], v[42:45], v[2:17]
	v_bitop3_b32 v34, v67, v90, 12 bitop3:0x36
	v_lshl_or_b32 v57, v34, 4, v89
	ds_read_b128 v[34:37], v57
	global_load_dwordx4 v[42:45], v[86:87], off offset:-4096
	s_waitcnt vmcnt(3) lgkmcnt(0)
	v_mfma_f32_32x32x16_f16 v[2:17], v[34:37], v[62:65], v[2:17]
	v_bitop3_b32 v34, v67, v71, 14 bitop3:0x36
	v_lshl_or_b32 v55, v34, 4, v88
	global_load_dwordx4 v[34:37], v[86:87], off
	v_mfma_f32_32x32x16_f16 v[18:33], v[82:85], v[62:65], v[18:33]
	ds_read_b128 v[60:63], v55
	v_add_co_u32_e32 v64, vcc, s0, v68
	s_mov_b32 s0, 0xf000
	s_nop 0
	v_addc_co_u32_e32 v65, vcc, 0, v69, vcc
	s_waitcnt vmcnt(3) lgkmcnt(0)
	v_mfma_f32_32x32x16_f16 v[18:33], v[60:63], v[50:53], v[18:33]
	ds_read_b128 v[60:63], v54
	s_waitcnt lgkmcnt(0)
	v_mfma_f32_32x32x16_f16 v[2:17], v[60:63], v[50:53], v[2:17]
	global_load_dwordx4 v[60:63], v[64:65], off offset:-4096
	ds_read_b128 v[50:53], v80 offset:15360
	global_load_dwordx4 v[38:41], v[38:39], off
	s_waitcnt vmcnt(4) lgkmcnt(0)
	v_mfma_f32_32x32x16_f16 v[18:33], v[50:53], v[46:49], v[18:33]
	ds_read_b128 v[50:53], v81 offset:15360
	s_waitcnt lgkmcnt(0)
	v_mfma_f32_32x32x16_f16 v[2:17], v[50:53], v[46:49], v[2:17]
	ds_read_b128 v[46:49], v78 offset:15360
	global_load_dwordx4 v[50:53], v[64:65], off
	v_add_co_u32_e32 v64, vcc, s0, v68
	s_nop 1
	v_addc_co_u32_e32 v65, vcc, 0, v69, vcc
	v_cmp_gt_u32_e32 vcc, 32, v66
	s_waitcnt vmcnt(1) lgkmcnt(0)
	v_mfma_f32_32x32x16_f16 v[18:33], v[46:49], v[38:41], v[18:33]
	ds_read_b128 v[46:49], v79 offset:15360
	s_waitcnt lgkmcnt(0)
	v_mfma_f32_32x32x16_f16 v[2:17], v[46:49], v[38:41], v[2:17]
	ds_read_b128 v[38:41], v77 offset:15360
	global_load_dwordx4 v[46:49], v[64:65], off offset:-4096
	s_waitcnt lgkmcnt(0)
	v_mfma_f32_32x32x16_f16 v[18:33], v[38:41], v[42:45], v[18:33]
	ds_read_b128 v[38:41], v76 offset:15360
	s_waitcnt lgkmcnt(0)
	v_mfma_f32_32x32x16_f16 v[2:17], v[38:41], v[42:45], v[2:17]
	ds_read_b128 v[42:45], v74 offset:15360
	global_load_dwordx4 v[38:41], v[64:65], off
	s_waitcnt lgkmcnt(0)
	v_mfma_f32_32x32x16_f16 v[18:33], v[42:45], v[34:37], v[18:33]
	ds_read_b128 v[42:45], v75 offset:15360
	s_waitcnt lgkmcnt(0)
	v_mfma_f32_32x32x16_f16 v[2:17], v[42:45], v[34:37], v[2:17]
	ds_read_b128 v[34:37], v72 offset:15360
	s_waitcnt lgkmcnt(0)
	v_mfma_f32_32x32x16_f16 v[18:33], v[34:37], v[60:63], v[18:33]
	ds_read_b128 v[34:37], v73 offset:15360
	s_waitcnt lgkmcnt(0)
	v_mfma_f32_32x32x16_f16 v[2:17], v[34:37], v[60:63], v[2:17]
	ds_read_b128 v[34:37], v58 offset:15360
	s_waitcnt vmcnt(2) lgkmcnt(0)
	v_mfma_f32_32x32x16_f16 v[18:33], v[34:37], v[50:53], v[18:33]
	ds_read_b128 v[34:37], v59 offset:15360
	s_waitcnt lgkmcnt(0)
	v_mfma_f32_32x32x16_f16 v[2:17], v[34:37], v[50:53], v[2:17]
	ds_read_b128 v[34:37], v56 offset:15360
	s_waitcnt vmcnt(1) lgkmcnt(0)
	v_mfma_f32_32x32x16_f16 v[18:33], v[34:37], v[46:49], v[18:33]
	ds_read_b128 v[34:37], v57 offset:15360
	s_waitcnt lgkmcnt(0)
	v_mfma_f32_32x32x16_f16 v[2:17], v[34:37], v[46:49], v[2:17]
	ds_read_b128 v[34:37], v55 offset:15360
	s_waitcnt vmcnt(0) lgkmcnt(0)
	v_mfma_f32_32x32x16_f16 v[18:33], v[34:37], v[38:41], v[18:33]
	ds_read_b128 v[34:37], v54 offset:15360
	s_waitcnt lgkmcnt(0)
	s_barrier
	s_nop 8
	v_add_f32_e32 v42, v70, v18
	v_mfma_f32_32x32x16_f16 v[2:17], v[34:37], v[38:41], v[2:17]
	v_lshlrev_b32_e32 v18, 11, v67
	v_or_b32_e32 v43, v1, v18
	v_add_f32_e32 v19, v70, v19
	ds_write2st64_b32 v43, v42, v19 offset1:2
	v_add_f32_e32 v19, v70, v20
	s_nop 6
	v_add_f32_e32 v3, v70, v3
	v_add_f32_e32 v4, v70, v4
	ds_write2st64_b32 v43, v3, v4 offset0:66 offset1:68
	v_add_f32_e32 v3, v70, v21
	ds_write2st64_b32 v43, v19, v3 offset0:4 offset1:6
	v_add_f32_e32 v3, v70, v5
	v_add_f32_e32 v5, v70, v6
	v_add_f32_e32 v4, v70, v22
	ds_write2st64_b32 v43, v3, v5 offset0:70 offset1:80
	v_add_f32_e32 v3, v70, v23
	ds_write2st64_b32 v43, v4, v3 offset0:16 offset1:18
	v_add_f32_e32 v3, v70, v7
	v_add_f32_e32 v5, v70, v8
	v_add_f32_e32 v4, v70, v24
	ds_write2st64_b32 v43, v3, v5 offset0:82 offset1:84
	v_add_f32_e32 v3, v70, v25
	ds_write2st64_b32 v43, v4, v3 offset0:20 offset1:22
	v_add_f32_e32 v3, v70, v9
	v_add_f32_e32 v5, v70, v10
	v_add_f32_e32 v4, v70, v26
	ds_write2st64_b32 v43, v3, v5 offset0:86 offset1:96
	v_add_f32_e32 v3, v70, v27
	ds_write2st64_b32 v43, v4, v3 offset0:32 offset1:34
	v_add_f32_e32 v3, v70, v11
	v_add_f32_e32 v5, v70, v12
	v_add_f32_e32 v4, v70, v28
	ds_write2st64_b32 v43, v3, v5 offset0:98 offset1:100
	v_add_f32_e32 v3, v70, v29
	ds_write2st64_b32 v43, v4, v3 offset0:36 offset1:38
	v_add_f32_e32 v3, v70, v13
	v_add_f32_e32 v2, v70, v2
	ds_write_b32 v43, v3 offset:26112
	v_add_f32_e32 v3, v70, v30
	ds_write2st64_b32 v43, v3, v2 offset0:48 offset1:64
	s_and_saveexec_b64 s[0:1], vcc
	v_add_f32_e32 v2, v70, v14
	ds_write_b32 v1, v2 offset:28672
	s_or_b64 exec, exec, s[0:1]
	v_lshlrev_b32_e32 v3, 2, v67
	v_add_f32_e32 v4, v70, v31
	v_add_u32_e32 v2, v1, v18
	ds_write_b32 v2, v4 offset:12800
	v_or_b32_e32 v4, 57, v3
	v_cmp_gt_u32_e64 s[0:1], 60, v4
	s_and_saveexec_b64 s[4:5], s[0:1]
	v_lshl_or_b32 v4, v4, 9, v1
	v_add_f32_e32 v5, v70, v15
	ds_write_b32 v4, v5
	s_or_b64 exec, exec, s[4:5]
	v_or_b32_e32 v3, 58, v3
	v_add_f32_e32 v4, v70, v32
	v_cmp_gt_u32_e64 s[0:1], 60, v3
	ds_write_b32 v2, v4 offset:13312
	s_and_saveexec_b64 s[4:5], s[0:1]
	v_lshl_or_b32 v3, v3, 9, v1
	v_add_f32_e32 v4, v70, v16
	ds_write_b32 v3, v4
	s_or_b64 exec, exec, s[4:5]
	v_add_f32_e32 v3, v70, v33
	ds_write_b32 v2, v3 offset:13824
	s_and_saveexec_b64 s[0:1], vcc
	v_add_f32_e32 v2, v70, v17
	ds_write_b32 v1, v2 offset:30208
	s_or_b64 exec, exec, s[0:1]
	v_lshlrev_b32_e32 v1, 4, v0
	v_and_b32_e32 v4, 0x1f0, v1
	v_mov_b32_e32 v5, 0
	v_lshrrev_b32_e32 v1, 5, v0
	v_lshl_add_u64 v[2:3], s[2:3], 0, v[4:5]
	v_add_u32_e32 v6, s16, v1
	s_mov_b32 s2, 0x186a0
	v_cmp_gt_i32_e32 vcc, s2, v6
	s_waitcnt lgkmcnt(0)
	s_barrier
	s_and_saveexec_b64 s[0:1], vcc
	s_cbranch_execz .LBB3_71
	v_lshl_or_b32 v1, v1, 9, v4
	ds_read_b128 v[8:11], v1
	v_ashrrev_i32_e32 v7, 31, v6
	v_lshlrev_b64 v[6:7], 9, v[6:7]
	v_lshl_add_u64 v[6:7], v[2:3], 0, v[6:7]
	s_waitcnt lgkmcnt(0)
	global_store_dwordx4 v[6:7], v[8:11], off sc1
.LBB3_71:
	s_or_b64 exec, exec, s[0:1]
	v_or_b32_e32 v1, 0x100, v0
	v_lshrrev_b32_e32 v1, 5, v1
	v_add_u32_e32 v6, s16, v1
	v_cmp_gt_i32_e32 vcc, s2, v6
	s_and_saveexec_b64 s[0:1], vcc
	s_cbranch_execz .LBB3_73
	v_lshl_or_b32 v1, v1, 9, v4
	ds_read_b128 v[8:11], v1
	v_ashrrev_i32_e32 v7, 31, v6
	v_lshlrev_b64 v[6:7], 9, v[6:7]
	v_lshl_add_u64 v[6:7], v[2:3], 0, v[6:7]
	s_waitcnt lgkmcnt(0)
	global_store_dwordx4 v[6:7], v[8:11], off sc1
.LBB3_73:
	s_or_b64 exec, exec, s[0:1]
	v_or_b32_e32 v1, 0x200, v0
	v_lshrrev_b32_e32 v1, 5, v1
	v_add_u32_e32 v6, s16, v1
	v_cmp_gt_i32_e32 vcc, s2, v6
	s_and_saveexec_b64 s[0:1], vcc
	s_cbranch_execz .LBB3_75
	v_lshl_or_b32 v1, v1, 9, v4
	ds_read_b128 v[8:11], v1
	v_ashrrev_i32_e32 v7, 31, v6
	v_lshlrev_b64 v[6:7], 9, v[6:7]
	v_lshl_add_u64 v[6:7], v[2:3], 0, v[6:7]
	s_waitcnt lgkmcnt(0)
	global_store_dwordx4 v[6:7], v[8:11], off sc1
.LBB3_75:
	s_or_b64 exec, exec, s[0:1]
	v_or_b32_e32 v1, 0x300, v0
	v_lshrrev_b32_e32 v1, 5, v1
	v_add_u32_e32 v6, s16, v1
	v_cmp_gt_i32_e32 vcc, s2, v6
	s_and_saveexec_b64 s[0:1], vcc
	s_cbranch_execz .LBB3_77
	v_lshl_or_b32 v1, v1, 9, v4
	ds_read_b128 v[8:11], v1
	v_ashrrev_i32_e32 v7, 31, v6
	v_lshlrev_b64 v[6:7], 9, v[6:7]
	v_lshl_add_u64 v[6:7], v[2:3], 0, v[6:7]
	s_waitcnt lgkmcnt(0)
	global_store_dwordx4 v[6:7], v[8:11], off sc1
.LBB3_77:
	s_or_b64 exec, exec, s[0:1]
	v_or_b32_e32 v6, 0x400, v0
	v_lshrrev_b32_e32 v5, 5, v6
	s_movk_i32 s0, 0x780
	v_add_u32_e32 v7, s16, v5
	v_mov_b32_e32 v1, 0x186a0
	v_cmp_gt_u32_e32 vcc, s0, v6
	s_nop 1
	v_cndmask_b32_e32 v6, v1, v7, vcc
	v_cmp_gt_i32_e32 vcc, s2, v6
	s_and_saveexec_b64 s[0:1], vcc
	s_cbranch_execz .LBB3_79
	v_min_u32_e32 v5, 59, v5
	v_lshl_or_b32 v5, v5, 9, v4
	ds_read_b128 v[8:11], v5
	v_ashrrev_i32_e32 v7, 31, v6
	v_lshlrev_b64 v[6:7], 9, v[6:7]
	v_lshl_add_u64 v[6:7], v[2:3], 0, v[6:7]
	s_waitcnt lgkmcnt(0)
	global_store_dwordx4 v[6:7], v[8:11], off sc1
.LBB3_79:
	s_or_b64 exec, exec, s[0:1]
	v_or_b32_e32 v5, 0x500, v0
	v_lshrrev_b32_e32 v5, 5, v5
	s_movk_i32 s0, 0x280
	v_add_u32_e32 v6, s16, v5
	v_cmp_gt_u32_e32 vcc, s0, v0
	s_nop 1
	v_cndmask_b32_e32 v6, v1, v6, vcc
	v_cmp_gt_i32_e32 vcc, s2, v6
	s_and_saveexec_b64 s[0:1], vcc
	s_cbranch_execz .LBB3_81
	v_min_u32_e32 v1, 59, v5
	v_lshl_or_b32 v1, v1, 9, v4
	ds_read_b128 v[8:11], v1
	v_ashrrev_i32_e32 v7, 31, v6
	v_lshlrev_b64 v[6:7], 9, v[6:7]
	v_lshl_add_u64 v[6:7], v[2:3], 0, v[6:7]
	s_waitcnt lgkmcnt(0)
	global_store_dwordx4 v[6:7], v[8:11], off sc1
.LBB3_81:
	s_or_b64 exec, exec, s[0:1]
	v_or_b32_e32 v1, 0x600, v0
	v_lshrrev_b32_e32 v5, 5, v1
	s_movk_i32 s0, 0x180
	v_add_u32_e32 v6, s16, v5
	v_mov_b32_e32 v1, 0x186a0
	v_cmp_gt_u32_e32 vcc, s0, v0
	s_nop 1
	v_cndmask_b32_e32 v6, v1, v6, vcc
	v_cmp_gt_i32_e32 vcc, s2, v6
	s_and_saveexec_b64 s[0:1], vcc
	s_cbranch_execz .LBB3_83
	v_min_u32_e32 v5, 59, v5
	v_lshl_or_b32 v5, v5, 9, v4
	ds_read_b128 v[8:11], v5
	v_ashrrev_i32_e32 v7, 31, v6
	v_lshlrev_b64 v[6:7], 9, v[6:7]
	v_lshl_add_u64 v[6:7], v[2:3], 0, v[6:7]
	s_waitcnt lgkmcnt(0)
	global_store_dwordx4 v[6:7], v[8:11], off sc1
.LBB3_83:
	s_or_b64 exec, exec, s[0:1]
	v_or_b32_e32 v5, 0x700, v0
	v_lshrrev_b32_e32 v5, 5, v5
	s_movk_i32 s0, 0x80
	v_add_u32_e32 v6, s16, v5
	v_cmp_gt_u32_e32 vcc, s0, v0
	s_nop 1
	v_cndmask_b32_e32 v0, v1, v6, vcc
	v_cmp_gt_i32_e32 vcc, s2, v0
	s_and_saveexec_b64 s[0:1], vcc
	s_cbranch_execz .LBB3_85
	v_min_u32_e32 v1, 59, v5
	v_lshl_or_b32 v1, v1, 9, v4
	ds_read_b128 v[4:7], v1
	v_ashrrev_i32_e32 v1, 31, v0
	v_lshlrev_b64 v[0:1], 9, v[0:1]
	v_lshl_add_u64 v[0:1], v[2:3], 0, v[0:1]
	s_waitcnt lgkmcnt(0)
	global_store_dwordx4 v[0:1], v[4:7], off sc1
